# v6 + P0 rmsnorm rows: gain vector in registers, counted waits keep the next row's loads in flight
# speedup vs baseline: 1.0155x; 1.0155x over previous
.LBB0_61:
	v_readlane_b32 s2, v252, 37
	v_readlane_b32 s3, v252, 38
	s_and_b64 s[0:1], s[2:3], exec
	v_readlane_b32 s0, v252, 14
	s_cselect_b32 s0, s0, s9
	s_cmpk_gt_i32 s0, 0x3fff
	s_cbranch_scc1 .LBB0_70
	s_and_b64 s[2:3], s[2:3], exec
	s_cselect_b32 s19, s85, s8
	s_ashr_i32 s1, s0, 31
	s_lshl_b64 s[2:3], s[0:1], 13
	v_readlane_b32 s20, v252, 21
	v_readlane_b32 s21, v252, 22
	s_add_u32 s2, s20, s2
	s_waitcnt vmcnt(21)
	v_lshlrev_b64 v[66:67], 4, v[198:199]
	s_addc_u32 s3, s21, s3
	v_lshl_add_u64 v[18:19], s[2:3], 0, v[66:67]
	s_movk_i32 s2, 0x1000
	v_add_co_u32_e32 v34, vcc, s2, v18
	global_load_dwordx4 v[2:5], v[18:19], off
	global_load_dwordx4 v[6:9], v[18:19], off offset:1024
	global_load_dwordx4 v[10:13], v[18:19], off offset:2048
	global_load_dwordx4 v[14:17], v[18:19], off offset:3072
	v_addc_co_u32_e32 v35, vcc, 0, v19, vcc
	global_load_dwordx4 v[18:21], v[34:35], off
	global_load_dwordx4 v[22:25], v[34:35], off offset:1024
	global_load_dwordx4 v[26:29], v[34:35], off offset:2048
	global_load_dwordx4 v[30:33], v[34:35], off offset:3072
	v_mbcnt_lo_u32_b32 v1, -1, 0
	v_mbcnt_hi_u32_b32 v34, -1, v1
	v_and_b32_e32 v1, 64, v34
	v_add_u32_e32 v35, 64, v1
	v_xor_b32_e32 v1, 1, v34
	v_cmp_lt_i32_e32 vcc, v1, v35
	v_xor_b32_e32 v36, 2, v34
	v_readlane_b32 s26, v252, 27
	v_cndmask_b32_e32 v1, v34, v1, vcc
	v_cmp_lt_i32_e32 vcc, v36, v35
	v_readlane_b32 s27, v252, 28
	s_mov_b64 s[4:5], 0x1000
	v_cndmask_b32_e32 v36, v34, v36, vcc
	s_waitcnt vmcnt(17)
	v_lshlrev_b32_e32 v87, 2, v36
	v_xor_b32_e32 v36, 4, v34
	v_cmp_lt_i32_e32 vcc, v36, v35
	v_lshl_add_u64 v[68:69], s[26:27], 0, v[66:67]
	v_lshl_add_u64 v[70:71], v[68:69], 0, s[4:5]
	v_cndmask_b32_e32 v36, v34, v36, vcc
	v_lshlrev_b32_e32 v92, 2, v36
	v_xor_b32_e32 v36, 8, v34
	v_cmp_lt_i32_e32 vcc, v36, v35
	s_mov_b64 s[4:5], 0x1400
	v_lshl_add_u64 v[72:73], v[68:69], 0, s[4:5]
	v_cndmask_b32_e32 v36, v34, v36, vcc
	v_lshlrev_b32_e32 v93, 2, v36
	v_xor_b32_e32 v36, 16, v34
	v_cmp_lt_i32_e32 vcc, v36, v35
	s_mov_b64 s[4:5], 0x1800
	s_add_i32 s8, s19, s0
	v_cndmask_b32_e32 v36, v34, v36, vcc
	v_lshlrev_b32_e32 v94, 2, v36
	v_xor_b32_e32 v36, 32, v34
	v_cmp_lt_i32_e32 vcc, v36, v35
	s_lshl_b32 s2, s19, 1
	v_lshl_add_u64 v[74:75], v[68:69], 0, s[4:5]
	v_cndmask_b32_e32 v34, v34, v36, vcc
	s_mov_b64 s[4:5], 0x1c00
	s_ashr_i32 s9, s8, 31
	v_lshlrev_b32_e32 v95, 2, v34
	v_lshl_add_u64 v[76:77], v[68:69], 0, s[4:5]
	global_load_dwordx4 v[200:203], v[68:69], off
	global_load_dwordx4 v[204:207], v[68:69], off offset:1024
	global_load_dwordx4 v[208:211], v[68:69], off offset:2048
	global_load_dwordx4 v[212:215], v[68:69], off offset:3072
	global_load_dwordx4 v[216:219], v[70:71], off
	global_load_dwordx4 v[220:223], v[72:73], off
	global_load_dwordx4 v[224:227], v[74:75], off
	global_load_dwordx4 v[228:231], v[76:77], off
	s_waitcnt vmcnt(0)
	s_lshl_b64 s[4:5], s[0:1], 11
	v_lshlrev_b64 v[34:35], 2, v[198:199]
	s_ashr_i32 s3, s2, 31
	s_lshl_b64 s[6:7], s[0:1], 12
	v_lshlrev_b64 v[36:37], 3, v[198:199]
	s_lshl_b64 s[10:11], s[8:9], 11
	v_lshl_add_u64 v[78:79], s[4:5], 0, v[34:35]
	s_lshl_b64 s[4:5], s[2:3], 11
	s_waitcnt vmcnt(16)
	v_lshl_add_u64 v[80:81], s[6:7], 0, v[36:37]
	s_lshl_b64 s[6:7], s[2:3], 12
	v_lshl_add_u64 v[82:83], s[10:11], 0, v[34:35]
	s_lshl_b64 s[10:11], s[8:9], 12
	s_lshl_b64 s[8:9], s[8:9], 13
	v_lshl_add_u64 v[84:85], s[10:11], 0, v[36:37]
	s_add_u32 s10, s20, s8
	s_addc_u32 s11, s21, s9
	s_add_i32 s8, s0, s2
	s_ashr_i32 s9, s8, 31
	s_lshl_b64 s[12:13], s[2:3], 13
	s_lshl_b64 s[8:9], s[8:9], 13
	s_add_u32 s14, s20, s8
	v_lshlrev_b32_e32 v1, 2, v1
	s_addc_u32 s15, s21, s9
	v_mov_b32_e32 v96, 0x358637bd
	s_mov_b32 s1, 0xf800000
	v_mov_b32_e32 v97, 0x260
	s_movk_i32 s3, 0x7fff
	s_mov_b32 s20, 0x38a00000
	s_mov_b32 s21, 0xc6800000
	v_mov_b32_e32 v98, 1
	v_readlane_b32 s22, v252, 23
	v_readlane_b32 s23, v252, 24
	v_readlane_b32 s24, v252, 25
	v_readlane_b32 s25, v252, 26
	s_waitcnt vmcnt(0)
	s_branch .LBB0_65
.LBB0_63:
	v_mov_b32_e32 v90, v35
	v_mov_b32_e32 v91, v39
	v_mov_b32_e32 v88, v34
	v_mov_b32_e32 v89, v38
	v_pk_mul_f32 v[90:91], v[90:91], v[90:91]
	v_mov_b32_e32 v100, v37
	v_mov_b32_e32 v101, v41
	v_pk_fma_f32 v[88:89], v[88:89], v[88:89], v[90:91]
	v_mov_b32_e32 v90, v36
	v_mov_b32_e32 v91, v40
	v_pk_mul_f32 v[100:101], v[100:101], v[100:101]
	v_mul_f32_e32 v86, v50, v50
	v_pk_fma_f32 v[90:91], v[90:91], v[90:91], v[100:101]
	v_pk_mul_f32 v[100:101], v[42:43], v[42:43]
	v_pk_add_f32 v[88:89], v[88:89], v[90:91]
	v_pk_mul_f32 v[90:91], v[44:45], v[44:45]
	v_mul_f32_e32 v99, v51, v51
	v_pk_mov_b32 v[102:103], v[100:101], v[90:91] op_sel:[1,0]
	v_mov_b32_e32 v101, v91
	v_pk_add_f32 v[90:91], v[102:103], v[100:101]
	v_pk_add_f32 v[88:89], v[88:89], v[88:89] op_sel:[0,1] op_sel_hi:[1,0]
	v_pk_add_f32 v[90:91], v[90:91], v[90:91] op_sel:[0,1] op_sel_hi:[1,0]
	v_mov_b32_e32 v89, v86
	v_mov_b32_e32 v91, v99
	v_mul_f32_e32 v86, v47, v47
	v_mul_f32_e32 v100, v52, v52
	v_pk_add_f32 v[88:89], v[88:89], v[90:91]
	v_pk_fma_f32 v[90:91], v[46:47], v[46:47], v[86:87] op_sel_hi:[1,1,0]
	v_mul_f32_e32 v86, v49, v49
	v_mul_f32_e32 v102, v53, v53
	v_mov_b32_e32 v91, v100
	v_pk_fma_f32 v[100:101], v[48:49], v[48:49], v[86:87] op_sel_hi:[1,1,0]
	v_mul_f32_e32 v86, v62, v62
	v_mov_b32_e32 v101, v102
	v_pk_add_f32 v[90:91], v[90:91], v[100:101]
	v_pk_mul_f32 v[100:101], v[54:55], v[54:55]
	v_pk_add_f32 v[88:89], v[88:89], v[90:91]
	v_pk_mul_f32 v[90:91], v[56:57], v[56:57]
	v_mul_f32_e32 v99, v63, v63
	v_pk_mov_b32 v[102:103], v[100:101], v[90:91] op_sel:[1,0]
	v_mov_b32_e32 v101, v91
	v_pk_add_f32 v[90:91], v[102:103], v[100:101]
	v_pk_add_f32 v[88:89], v[88:89], v[88:89] op_sel:[0,1] op_sel_hi:[1,0]
	v_pk_add_f32 v[90:91], v[90:91], v[90:91] op_sel:[0,1] op_sel_hi:[1,0]
	v_mov_b32_e32 v89, v86
	v_mov_b32_e32 v91, v99
	v_mul_f32_e32 v86, v59, v59
	v_pk_add_f32 v[100:101], v[88:89], v[90:91]
	v_pk_fma_f32 v[88:89], v[58:59], v[58:59], v[86:87] op_sel_hi:[1,1,0]
	v_mul_f32_e32 v86, v61, v61
	v_mul_f32_e32 v102, v64, v64
	v_mul_f32_e32 v103, v65, v65
	v_pk_fma_f32 v[90:91], v[60:61], v[60:61], v[86:87] op_sel_hi:[1,1,0]
	v_mov_b32_e32 v89, v102
	v_mov_b32_e32 v91, v103
	v_pk_add_f32 v[102:103], v[88:89], v[90:91]
	v_mov_b64_e32 v[88:89], v[200:201]
	v_mov_b64_e32 v[90:91], v[202:203]
	v_pk_add_f32 v[100:101], v[100:101], v[102:103]
	s_nop 0
	v_add_f32_e32 v86, v100, v101
	ds_bpermute_b32 v99, v1, v86
	s_waitcnt lgkmcnt(0)
	v_add_f32_e32 v86, v86, v99
	ds_bpermute_b32 v99, v87, v86
	s_waitcnt lgkmcnt(0)
	v_add_f32_e32 v86, v86, v99
	ds_bpermute_b32 v99, v92, v86
	s_waitcnt lgkmcnt(0)
	v_add_f32_e32 v86, v86, v99
	ds_bpermute_b32 v99, v93, v86
	s_waitcnt lgkmcnt(0)
	v_add_f32_e32 v86, v86, v99
	ds_bpermute_b32 v99, v94, v86
	s_waitcnt lgkmcnt(0)
	v_add_f32_e32 v86, v86, v99
	ds_bpermute_b32 v99, v95, v86
	s_waitcnt lgkmcnt(0)
	v_add_f32_e32 v86, v86, v99
	v_fmamk_f32 v86, v86, 0x3a000000, v96
	v_mul_f32_e32 v99, 0x4f800000, v86
	v_cmp_gt_f32_e32 vcc, s1, v86
	s_nop 1
	v_cndmask_b32_e32 v86, v86, v99, vcc
	v_sqrt_f32_e32 v99, v86
	s_nop 0
	v_add_u32_e32 v100, -1, v99
	v_fma_f32 v101, -v100, v99, v86
	v_cmp_ge_f32_e64 s[8:9], 0, v101
	v_add_u32_e32 v101, 1, v99
	s_nop 0
	v_cndmask_b32_e64 v100, v99, v100, s[8:9]
	v_fma_f32 v99, -v101, v99, v86
	v_cmp_lt_f32_e64 s[8:9], 0, v99
	s_nop 1
	v_cndmask_b32_e64 v99, v100, v101, s[8:9]
	v_mul_f32_e32 v100, 0x37800000, v99
	v_cndmask_b32_e32 v99, v99, v100, vcc
	v_cmp_class_f32_e32 vcc, v86, v97
	s_nop 1
	v_cndmask_b32_e32 v86, v99, v86, vcc
	v_div_scale_f32 v99, s[8:9], v86, v86, 1.0
	v_rcp_f32_e32 v100, v99
	s_nop 0
	v_fma_f32 v101, -v99, v100, 1.0
	v_fmac_f32_e32 v100, v101, v100
	v_div_scale_f32 v101, vcc, 1.0, v86, 1.0
	v_mul_f32_e32 v102, v101, v100
	v_fma_f32 v103, -v99, v102, v101
	v_fmac_f32_e32 v102, v103, v100
	v_fma_f32 v99, -v99, v102, v101
	v_div_fmas_f32 v99, v99, v100, v102
	v_div_fixup_f32 v86, v99, v86, 1.0
	v_pk_mul_f32 v[106:107], v[86:87], v[36:37] op_sel_hi:[0,1]
	v_pk_mul_f32 v[104:105], v[86:87], v[34:35] op_sel_hi:[0,1]
	v_pk_mul_f32 v[90:91], v[106:107], v[90:91]
	v_pk_mul_f32 v[88:89], v[104:105], v[88:89]
	v_and_b32_sdwa v105, v91, v98 dst_sel:DWORD dst_unused:UNUSED_PAD src0_sel:WORD_1 src1_sel:DWORD
	v_and_b32_sdwa v99, v90, v98 dst_sel:DWORD dst_unused:UNUSED_PAD src0_sel:WORD_1 src1_sel:DWORD
	v_add3_u32 v105, v91, v105, s3
	v_add3_u32 v99, v90, v99, s3
	v_and_b32_e32 v105, 0xffff0000, v105
	v_or_b32_sdwa v105, v105, v99 dst_sel:DWORD dst_unused:UNUSED_PAD src0_sel:DWORD src1_sel:WORD_1
	v_mov_b32_e32 v99, 0
	v_cvt_pk_fp8_f32 v99, v88, v89
	v_lshl_add_u64 v[100:101], s[82:83], 0, v[84:85]
	v_and_b32_sdwa v104, v88, v98 dst_sel:DWORD dst_unused:UNUSED_PAD src0_sel:WORD_1 src1_sel:DWORD
	v_add3_u32 v104, v88, v104, s3
	v_and_b32_sdwa v106, v89, v98 dst_sel:DWORD dst_unused:UNUSED_PAD src0_sel:WORD_1 src1_sel:DWORD
	v_add_co_u32_e32 v88, vcc, s20, v100
	v_cvt_pk_fp8_f32 v99, v90, v91 op_sel:[0,0,1]
	v_lshl_add_u64 v[102:103], s[82:83], 0, v[82:83]
	v_add3_u32 v106, v89, v106, s3
	v_addc_co_u32_e32 v89, vcc, 0, v101, vcc
	v_and_b32_e32 v106, 0xffff0000, v106
	v_add_co_u32_e32 v90, vcc, s21, v102
	v_or_b32_sdwa v104, v106, v104 dst_sel:DWORD dst_unused:UNUSED_PAD src0_sel:DWORD src1_sel:WORD_1
	s_nop 0
	v_addc_co_u32_e32 v91, vcc, 0, v103, vcc
	global_store_dwordx2 v[88:89], v[104:105], off
	global_store_dword v[90:91], v99, off
	v_mov_b64_e32 v[100:101], v[204:205]
	v_mov_b64_e32 v[102:103], v[206:207]
	v_pk_mul_f32 v[104:105], v[86:87], v[38:39] op_sel_hi:[0,1]
	v_mov_b32_e32 v99, 0
	v_pk_mul_f32 v[106:107], v[86:87], v[40:41] op_sel_hi:[0,1]
	v_pk_mul_f32 v[100:101], v[104:105], v[100:101]
	s_nop 0
	v_cvt_pk_fp8_f32 v99, v100, v101
	v_pk_mul_f32 v[102:103], v[106:107], v[102:103]
	v_and_b32_sdwa v105, v100, v98 dst_sel:DWORD dst_unused:UNUSED_PAD src0_sel:WORD_1 src1_sel:DWORD
	v_and_b32_sdwa v106, v103, v98 dst_sel:DWORD dst_unused:UNUSED_PAD src0_sel:WORD_1 src1_sel:DWORD
	v_and_b32_sdwa v107, v101, v98 dst_sel:DWORD dst_unused:UNUSED_PAD src0_sel:WORD_1 src1_sel:DWORD
	v_and_b32_sdwa v104, v102, v98 dst_sel:DWORD dst_unused:UNUSED_PAD src0_sel:WORD_1 src1_sel:DWORD
	v_add3_u32 v100, v100, v105, s3
	v_add3_u32 v105, v103, v106, s3
	v_add3_u32 v101, v101, v107, s3
	v_cvt_pk_fp8_f32 v99, v102, v103 op_sel:[0,0,1]
	v_add3_u32 v104, v102, v104, s3
	v_and_b32_e32 v105, 0xffff0000, v105
	v_and_b32_e32 v106, 0xffff0000, v101
	v_or_b32_sdwa v101, v105, v104 dst_sel:DWORD dst_unused:UNUSED_PAD src0_sel:DWORD src1_sel:WORD_1
	v_or_b32_sdwa v100, v106, v100 dst_sel:DWORD dst_unused:UNUSED_PAD src0_sel:DWORD src1_sel:WORD_1
	global_store_dwordx2 v[88:89], v[100:101], off offset:512
	global_store_dword v[90:91], v99, off offset:256
	v_mov_b64_e32 v[100:101], v[208:209]
	v_mov_b64_e32 v[102:103], v[210:211]
	v_pk_mul_f32 v[104:105], v[86:87], v[42:43] op_sel_hi:[0,1]
	v_mov_b32_e32 v99, 0
	v_pk_mul_f32 v[106:107], v[86:87], v[44:45] op_sel_hi:[0,1]
	v_pk_mul_f32 v[100:101], v[104:105], v[100:101]
	s_nop 0
	v_cvt_pk_fp8_f32 v99, v100, v101
	v_pk_mul_f32 v[102:103], v[106:107], v[102:103]
	v_and_b32_sdwa v105, v100, v98 dst_sel:DWORD dst_unused:UNUSED_PAD src0_sel:WORD_1 src1_sel:DWORD
	v_and_b32_sdwa v106, v103, v98 dst_sel:DWORD dst_unused:UNUSED_PAD src0_sel:WORD_1 src1_sel:DWORD
	v_and_b32_sdwa v107, v101, v98 dst_sel:DWORD dst_unused:UNUSED_PAD src0_sel:WORD_1 src1_sel:DWORD
	v_and_b32_sdwa v104, v102, v98 dst_sel:DWORD dst_unused:UNUSED_PAD src0_sel:WORD_1 src1_sel:DWORD
	v_add3_u32 v100, v100, v105, s3
	v_add3_u32 v105, v103, v106, s3
	v_add3_u32 v101, v101, v107, s3
	v_cvt_pk_fp8_f32 v99, v102, v103 op_sel:[0,0,1]
	v_add3_u32 v104, v102, v104, s3
	v_and_b32_e32 v105, 0xffff0000, v105
	v_and_b32_e32 v106, 0xffff0000, v101
	v_or_b32_sdwa v101, v105, v104 dst_sel:DWORD dst_unused:UNUSED_PAD src0_sel:DWORD src1_sel:WORD_1
	v_or_b32_sdwa v100, v106, v100 dst_sel:DWORD dst_unused:UNUSED_PAD src0_sel:DWORD src1_sel:WORD_1
	global_store_dwordx2 v[88:89], v[100:101], off offset:1024
	global_store_dword v[90:91], v99, off offset:512
	v_mov_b64_e32 v[100:101], v[212:213]
	v_mov_b64_e32 v[102:103], v[214:215]
	v_pk_mul_f32 v[104:105], v[86:87], v[46:47] op_sel_hi:[0,1]
	v_mov_b32_e32 v99, 0
	v_pk_mul_f32 v[106:107], v[86:87], v[48:49] op_sel_hi:[0,1]
	v_pk_mul_f32 v[100:101], v[104:105], v[100:101]
	s_nop 0
	v_cvt_pk_fp8_f32 v99, v100, v101
	v_pk_mul_f32 v[102:103], v[106:107], v[102:103]
	v_and_b32_sdwa v105, v100, v98 dst_sel:DWORD dst_unused:UNUSED_PAD src0_sel:WORD_1 src1_sel:DWORD
	v_and_b32_sdwa v106, v103, v98 dst_sel:DWORD dst_unused:UNUSED_PAD src0_sel:WORD_1 src1_sel:DWORD
	v_and_b32_sdwa v107, v101, v98 dst_sel:DWORD dst_unused:UNUSED_PAD src0_sel:WORD_1 src1_sel:DWORD
	v_and_b32_sdwa v104, v102, v98 dst_sel:DWORD dst_unused:UNUSED_PAD src0_sel:WORD_1 src1_sel:DWORD
	v_add3_u32 v100, v100, v105, s3
	v_add3_u32 v105, v103, v106, s3
	v_add3_u32 v101, v101, v107, s3
	v_cvt_pk_fp8_f32 v99, v102, v103 op_sel:[0,0,1]
	v_add3_u32 v104, v102, v104, s3
	v_and_b32_e32 v105, 0xffff0000, v105
	v_and_b32_e32 v106, 0xffff0000, v101
	v_or_b32_sdwa v101, v105, v104 dst_sel:DWORD dst_unused:UNUSED_PAD src0_sel:DWORD src1_sel:WORD_1
	v_or_b32_sdwa v100, v106, v100 dst_sel:DWORD dst_unused:UNUSED_PAD src0_sel:DWORD src1_sel:WORD_1
	global_store_dwordx2 v[88:89], v[100:101], off offset:1536
	global_store_dword v[90:91], v99, off offset:768
	v_mov_b64_e32 v[100:101], v[216:217]
	v_mov_b64_e32 v[102:103], v[218:219]
	v_pk_mul_f32 v[104:105], v[86:87], v[50:51] op_sel_hi:[0,1]
	v_mov_b32_e32 v99, 0
	v_pk_mul_f32 v[106:107], v[86:87], v[52:53] op_sel_hi:[0,1]
	v_pk_mul_f32 v[100:101], v[104:105], v[100:101]
	s_nop 0
	v_cvt_pk_fp8_f32 v99, v100, v101
	v_pk_mul_f32 v[102:103], v[106:107], v[102:103]
	v_and_b32_sdwa v105, v100, v98 dst_sel:DWORD dst_unused:UNUSED_PAD src0_sel:WORD_1 src1_sel:DWORD
	v_and_b32_sdwa v106, v103, v98 dst_sel:DWORD dst_unused:UNUSED_PAD src0_sel:WORD_1 src1_sel:DWORD
	v_and_b32_sdwa v107, v101, v98 dst_sel:DWORD dst_unused:UNUSED_PAD src0_sel:WORD_1 src1_sel:DWORD
	v_and_b32_sdwa v104, v102, v98 dst_sel:DWORD dst_unused:UNUSED_PAD src0_sel:WORD_1 src1_sel:DWORD
	v_add3_u32 v100, v100, v105, s3
	v_add3_u32 v105, v103, v106, s3
	v_add3_u32 v101, v101, v107, s3
	v_cvt_pk_fp8_f32 v99, v102, v103 op_sel:[0,0,1]
	v_add3_u32 v104, v102, v104, s3
	v_and_b32_e32 v105, 0xffff0000, v105
	v_and_b32_e32 v106, 0xffff0000, v101
	v_or_b32_sdwa v101, v105, v104 dst_sel:DWORD dst_unused:UNUSED_PAD src0_sel:DWORD src1_sel:WORD_1
	v_or_b32_sdwa v100, v106, v100 dst_sel:DWORD dst_unused:UNUSED_PAD src0_sel:DWORD src1_sel:WORD_1
	global_store_dwordx2 v[88:89], v[100:101], off offset:2048
	global_store_dword v[90:91], v99, off offset:1024
	v_mov_b64_e32 v[100:101], v[220:221]
	v_mov_b64_e32 v[102:103], v[222:223]
	v_pk_mul_f32 v[104:105], v[86:87], v[54:55] op_sel_hi:[0,1]
	v_mov_b32_e32 v99, 0
	v_pk_mul_f32 v[106:107], v[86:87], v[56:57] op_sel_hi:[0,1]
	v_pk_mul_f32 v[100:101], v[104:105], v[100:101]
	s_nop 0
	v_cvt_pk_fp8_f32 v99, v100, v101
	v_pk_mul_f32 v[102:103], v[106:107], v[102:103]
	v_and_b32_sdwa v105, v100, v98 dst_sel:DWORD dst_unused:UNUSED_PAD src0_sel:WORD_1 src1_sel:DWORD
	v_and_b32_sdwa v106, v103, v98 dst_sel:DWORD dst_unused:UNUSED_PAD src0_sel:WORD_1 src1_sel:DWORD
	v_and_b32_sdwa v107, v101, v98 dst_sel:DWORD dst_unused:UNUSED_PAD src0_sel:WORD_1 src1_sel:DWORD
	v_and_b32_sdwa v104, v102, v98 dst_sel:DWORD dst_unused:UNUSED_PAD src0_sel:WORD_1 src1_sel:DWORD
	v_add3_u32 v100, v100, v105, s3
	v_add3_u32 v105, v103, v106, s3
	v_add3_u32 v101, v101, v107, s3
	v_cvt_pk_fp8_f32 v99, v102, v103 op_sel:[0,0,1]
	v_add3_u32 v104, v102, v104, s3
	v_and_b32_e32 v105, 0xffff0000, v105
	v_and_b32_e32 v106, 0xffff0000, v101
	v_or_b32_sdwa v101, v105, v104 dst_sel:DWORD dst_unused:UNUSED_PAD src0_sel:DWORD src1_sel:WORD_1
	v_or_b32_sdwa v100, v106, v100 dst_sel:DWORD dst_unused:UNUSED_PAD src0_sel:DWORD src1_sel:WORD_1
	global_store_dwordx2 v[88:89], v[100:101], off offset:2560
	global_store_dword v[90:91], v99, off offset:1280
	v_mov_b64_e32 v[100:101], v[224:225]
	v_mov_b64_e32 v[102:103], v[226:227]
	v_pk_mul_f32 v[104:105], v[86:87], v[58:59] op_sel_hi:[0,1]
	v_mov_b32_e32 v99, 0
	v_pk_mul_f32 v[106:107], v[86:87], v[60:61] op_sel_hi:[0,1]
	v_pk_mul_f32 v[100:101], v[104:105], v[100:101]
	s_nop 0
	v_cvt_pk_fp8_f32 v99, v100, v101
	v_pk_mul_f32 v[102:103], v[106:107], v[102:103]
	v_and_b32_sdwa v105, v100, v98 dst_sel:DWORD dst_unused:UNUSED_PAD src0_sel:WORD_1 src1_sel:DWORD
	v_and_b32_sdwa v106, v103, v98 dst_sel:DWORD dst_unused:UNUSED_PAD src0_sel:WORD_1 src1_sel:DWORD
	v_and_b32_sdwa v107, v101, v98 dst_sel:DWORD dst_unused:UNUSED_PAD src0_sel:WORD_1 src1_sel:DWORD
	v_and_b32_sdwa v104, v102, v98 dst_sel:DWORD dst_unused:UNUSED_PAD src0_sel:WORD_1 src1_sel:DWORD
	v_add3_u32 v100, v100, v105, s3
	v_add3_u32 v105, v103, v106, s3
	v_add3_u32 v101, v101, v107, s3
	v_cvt_pk_fp8_f32 v99, v102, v103 op_sel:[0,0,1]
	v_add3_u32 v104, v102, v104, s3
	v_and_b32_e32 v105, 0xffff0000, v105
	v_and_b32_e32 v106, 0xffff0000, v101
	v_or_b32_sdwa v101, v105, v104 dst_sel:DWORD dst_unused:UNUSED_PAD src0_sel:DWORD src1_sel:WORD_1
	v_or_b32_sdwa v100, v106, v100 dst_sel:DWORD dst_unused:UNUSED_PAD src0_sel:DWORD src1_sel:WORD_1
	global_store_dwordx2 v[88:89], v[100:101], off offset:3072
	global_store_dword v[90:91], v99, off offset:1536
	v_mov_b64_e32 v[100:101], v[228:229]
	v_mov_b64_e32 v[102:103], v[230:231]
	v_pk_mul_f32 v[104:105], v[86:87], v[62:63] op_sel_hi:[0,1]
	v_mov_b32_e32 v99, 0
	v_pk_mul_f32 v[106:107], v[86:87], v[64:65] op_sel_hi:[0,1]
	v_pk_mul_f32 v[100:101], v[104:105], v[100:101]
	s_nop 0
	v_cvt_pk_fp8_f32 v99, v100, v101
	v_pk_mul_f32 v[102:103], v[106:107], v[102:103]
	v_and_b32_sdwa v104, v100, v98 dst_sel:DWORD dst_unused:UNUSED_PAD src0_sel:WORD_1 src1_sel:DWORD
	v_and_b32_sdwa v105, v103, v98 dst_sel:DWORD dst_unused:UNUSED_PAD src0_sel:WORD_1 src1_sel:DWORD
	v_and_b32_sdwa v106, v101, v98 dst_sel:DWORD dst_unused:UNUSED_PAD src0_sel:WORD_1 src1_sel:DWORD
	v_and_b32_sdwa v86, v102, v98 dst_sel:DWORD dst_unused:UNUSED_PAD src0_sel:WORD_1 src1_sel:DWORD
	v_add3_u32 v100, v100, v104, s3
	v_add3_u32 v104, v103, v105, s3
	v_add3_u32 v101, v101, v106, s3
	v_cvt_pk_fp8_f32 v99, v102, v103 op_sel:[0,0,1]
	v_add3_u32 v86, v102, v86, s3
	v_and_b32_e32 v104, 0xffff0000, v104
	v_and_b32_e32 v105, 0xffff0000, v101
	v_or_b32_sdwa v101, v104, v86 dst_sel:DWORD dst_unused:UNUSED_PAD src0_sel:DWORD src1_sel:WORD_1
	v_or_b32_sdwa v100, v105, v100 dst_sel:DWORD dst_unused:UNUSED_PAD src0_sel:DWORD src1_sel:WORD_1
	global_store_dwordx2 v[88:89], v[100:101], off offset:3584
	global_store_dword v[90:91], v99, off offset:1792

.LBB0_65:
	s_waitcnt vmcnt(16)
	s_add_i32 s8, s19, s0
	s_cmpk_lt_i32 s8, 0x4000
	s_cselect_b64 s[16:17], -1, 0
	s_cmpk_gt_i32 s8, 0x3fff
	s_cbranch_scc1 .LBB0_67
	v_lshl_add_u64 v[50:51], s[10:11], 0, v[66:67]
	v_add_co_u32_e32 v62, vcc, 0x1000, v50
	global_load_dwordx4 v[34:37], v[50:51], off
	global_load_dwordx4 v[38:41], v[50:51], off offset:1024
	global_load_dwordx4 v[42:45], v[50:51], off offset:2048
	global_load_dwordx4 v[46:49], v[50:51], off offset:3072
	v_addc_co_u32_e32 v63, vcc, 0, v51, vcc
	global_load_dwordx4 v[50:53], v[62:63], off
	global_load_dwordx4 v[54:57], v[62:63], off offset:1024
	global_load_dwordx4 v[58:61], v[62:63], off offset:2048
	s_nop 0
	global_load_dwordx4 v[62:65], v[62:63], off offset:3072
.LBB0_67:
	v_mov_b32_e32 v90, v3
	v_mov_b32_e32 v91, v7
	v_mov_b32_e32 v88, v2
	v_mov_b32_e32 v89, v6
	v_pk_mul_f32 v[90:91], v[90:91], v[90:91]
	v_mov_b32_e32 v100, v5
	v_mov_b32_e32 v101, v9
	v_pk_fma_f32 v[88:89], v[88:89], v[88:89], v[90:91]
	v_mov_b32_e32 v90, v4
	v_mov_b32_e32 v91, v8
	v_pk_mul_f32 v[100:101], v[100:101], v[100:101]
	v_mul_f32_e32 v86, v18, v18
	v_pk_fma_f32 v[90:91], v[90:91], v[90:91], v[100:101]
	v_pk_mul_f32 v[100:101], v[10:11], v[10:11]
	v_pk_add_f32 v[88:89], v[88:89], v[90:91]
	v_pk_mul_f32 v[90:91], v[12:13], v[12:13]
	v_mul_f32_e32 v99, v19, v19
	v_pk_mov_b32 v[102:103], v[100:101], v[90:91] op_sel:[1,0]
	v_mov_b32_e32 v101, v91
	v_pk_add_f32 v[90:91], v[102:103], v[100:101]
	v_pk_add_f32 v[88:89], v[88:89], v[88:89] op_sel:[0,1] op_sel_hi:[1,0]
	v_pk_add_f32 v[90:91], v[90:91], v[90:91] op_sel:[0,1] op_sel_hi:[1,0]
	v_mov_b32_e32 v89, v86
	v_mov_b32_e32 v91, v99
	v_mul_f32_e32 v86, v15, v15
	v_mul_f32_e32 v100, v20, v20
	v_pk_add_f32 v[88:89], v[88:89], v[90:91]
	v_pk_fma_f32 v[90:91], v[14:15], v[14:15], v[86:87] op_sel_hi:[1,1,0]
	v_mul_f32_e32 v86, v17, v17
	v_mul_f32_e32 v102, v21, v21
	v_mov_b32_e32 v91, v100
	v_pk_fma_f32 v[100:101], v[16:17], v[16:17], v[86:87] op_sel_hi:[1,1,0]
	v_mul_f32_e32 v86, v30, v30
	v_mov_b32_e32 v101, v102
	v_pk_add_f32 v[90:91], v[90:91], v[100:101]
	v_pk_mul_f32 v[100:101], v[22:23], v[22:23]
	v_pk_add_f32 v[88:89], v[88:89], v[90:91]
	v_pk_mul_f32 v[90:91], v[24:25], v[24:25]
	v_mul_f32_e32 v99, v31, v31
	v_pk_mov_b32 v[102:103], v[100:101], v[90:91] op_sel:[1,0]
	v_mov_b32_e32 v101, v91
	v_pk_add_f32 v[90:91], v[102:103], v[100:101]
	v_pk_add_f32 v[88:89], v[88:89], v[88:89] op_sel:[0,1] op_sel_hi:[1,0]
	v_pk_add_f32 v[90:91], v[90:91], v[90:91] op_sel:[0,1] op_sel_hi:[1,0]
	v_mov_b32_e32 v89, v86
	v_mov_b32_e32 v91, v99
	v_mul_f32_e32 v86, v27, v27
	v_pk_add_f32 v[100:101], v[88:89], v[90:91]
	v_pk_fma_f32 v[88:89], v[26:27], v[26:27], v[86:87] op_sel_hi:[1,1,0]
	v_mul_f32_e32 v86, v29, v29
	v_mul_f32_e32 v102, v32, v32
	v_mul_f32_e32 v103, v33, v33
	v_pk_fma_f32 v[90:91], v[28:29], v[28:29], v[86:87] op_sel_hi:[1,1,0]
	v_mov_b32_e32 v89, v102
	v_mov_b32_e32 v91, v103
	v_pk_add_f32 v[102:103], v[88:89], v[90:91]
	v_mov_b64_e32 v[88:89], v[200:201]
	v_mov_b64_e32 v[90:91], v[202:203]
	v_pk_add_f32 v[100:101], v[100:101], v[102:103]
	s_add_i32 s0, s2, s0
	v_add_f32_e32 v86, v100, v101
	ds_bpermute_b32 v99, v1, v86
	s_waitcnt lgkmcnt(0)
	v_add_f32_e32 v86, v86, v99
	ds_bpermute_b32 v99, v87, v86
	s_waitcnt lgkmcnt(0)
	v_add_f32_e32 v86, v86, v99
	ds_bpermute_b32 v99, v92, v86
	s_waitcnt lgkmcnt(0)
	v_add_f32_e32 v86, v86, v99
	ds_bpermute_b32 v99, v93, v86
	s_waitcnt lgkmcnt(0)
	v_add_f32_e32 v86, v86, v99
	ds_bpermute_b32 v99, v94, v86
	s_waitcnt lgkmcnt(0)
	v_add_f32_e32 v86, v86, v99
	ds_bpermute_b32 v99, v95, v86
	s_waitcnt lgkmcnt(0)
	v_add_f32_e32 v86, v86, v99
	v_fmamk_f32 v86, v86, 0x3a000000, v96
	v_mul_f32_e32 v99, 0x4f800000, v86
	v_cmp_gt_f32_e32 vcc, s1, v86
	s_nop 1
	v_cndmask_b32_e32 v86, v86, v99, vcc
	v_sqrt_f32_e32 v99, v86
	s_nop 0
	v_add_u32_e32 v100, -1, v99
	v_fma_f32 v101, -v100, v99, v86
	v_cmp_ge_f32_e64 s[8:9], 0, v101
	v_add_u32_e32 v101, 1, v99
	s_nop 0
	v_cndmask_b32_e64 v100, v99, v100, s[8:9]
	v_fma_f32 v99, -v101, v99, v86
	v_cmp_lt_f32_e64 s[8:9], 0, v99
	s_nop 1
	v_cndmask_b32_e64 v99, v100, v101, s[8:9]
	v_mul_f32_e32 v100, 0x37800000, v99
	v_cndmask_b32_e32 v99, v99, v100, vcc
	v_cmp_class_f32_e32 vcc, v86, v97
	s_nop 1
	v_cndmask_b32_e32 v86, v99, v86, vcc
	v_div_scale_f32 v99, s[8:9], v86, v86, 1.0
	v_rcp_f32_e32 v100, v99
	s_nop 0
	v_fma_f32 v101, -v99, v100, 1.0
	v_fmac_f32_e32 v100, v101, v100
	v_div_scale_f32 v101, vcc, 1.0, v86, 1.0
	v_mul_f32_e32 v102, v101, v100
	v_fma_f32 v103, -v99, v102, v101
	v_fmac_f32_e32 v102, v103, v100
	v_fma_f32 v99, -v99, v102, v101
	v_div_fmas_f32 v99, v99, v100, v102
	v_div_fixup_f32 v86, v99, v86, 1.0
	v_pk_mul_f32 v[106:107], v[86:87], v[4:5] op_sel_hi:[0,1]
	v_pk_mul_f32 v[106:107], v[106:107], v[90:91]
	v_pk_mul_f32 v[104:105], v[86:87], v[2:3] op_sel_hi:[0,1]
	v_and_b32_sdwa v99, v107, v98 dst_sel:DWORD dst_unused:UNUSED_PAD src0_sel:WORD_1 src1_sel:DWORD
	v_and_b32_sdwa v90, v106, v98 dst_sel:DWORD dst_unused:UNUSED_PAD src0_sel:WORD_1 src1_sel:DWORD
	v_add3_u32 v99, v107, v99, s3
	v_add3_u32 v90, v106, v90, s3
	v_and_b32_e32 v99, 0xffff0000, v99
	v_pk_mul_f32 v[88:89], v[104:105], v[88:89]
	v_or_b32_sdwa v105, v99, v90 dst_sel:DWORD dst_unused:UNUSED_PAD src0_sel:DWORD src1_sel:WORD_1
	v_mov_b32_e32 v99, 0
	v_cvt_pk_fp8_f32 v99, v88, v89
	v_and_b32_sdwa v104, v89, v98 dst_sel:DWORD dst_unused:UNUSED_PAD src0_sel:WORD_1 src1_sel:DWORD
	v_lshl_add_u64 v[100:101], s[82:83], 0, v[80:81]
	v_and_b32_sdwa v91, v88, v98 dst_sel:DWORD dst_unused:UNUSED_PAD src0_sel:WORD_1 src1_sel:DWORD
	v_add3_u32 v104, v89, v104, s3
	v_add3_u32 v91, v88, v91, s3
	v_and_b32_e32 v104, 0xffff0000, v104
	v_add_co_u32_e32 v90, vcc, s20, v100
	v_cvt_pk_fp8_f32 v99, v106, v107 op_sel:[0,0,1]
	v_lshl_add_u64 v[102:103], s[82:83], 0, v[78:79]
	v_or_b32_sdwa v104, v104, v91 dst_sel:DWORD dst_unused:UNUSED_PAD src0_sel:DWORD src1_sel:WORD_1
	v_addc_co_u32_e32 v91, vcc, 0, v101, vcc
	v_add_co_u32_e32 v88, vcc, s21, v102
	global_store_dwordx2 v[90:91], v[104:105], off
	s_nop 0
	v_addc_co_u32_e32 v89, vcc, 0, v103, vcc
	global_store_dword v[88:89], v99, off
	v_mov_b64_e32 v[100:101], v[204:205]
	v_mov_b64_e32 v[102:103], v[206:207]
	v_pk_mul_f32 v[104:105], v[86:87], v[6:7] op_sel_hi:[0,1]
	v_mov_b32_e32 v99, 0
	v_pk_mul_f32 v[106:107], v[86:87], v[8:9] op_sel_hi:[0,1]
	s_andn2_b64 vcc, exec, s[16:17]
	v_pk_mul_f32 v[100:101], v[104:105], v[100:101]
	s_nop 0
	v_cvt_pk_fp8_f32 v99, v100, v101
	v_pk_mul_f32 v[102:103], v[106:107], v[102:103]
	v_and_b32_sdwa v105, v100, v98 dst_sel:DWORD dst_unused:UNUSED_PAD src0_sel:WORD_1 src1_sel:DWORD
	v_and_b32_sdwa v106, v103, v98 dst_sel:DWORD dst_unused:UNUSED_PAD src0_sel:WORD_1 src1_sel:DWORD
	v_and_b32_sdwa v107, v101, v98 dst_sel:DWORD dst_unused:UNUSED_PAD src0_sel:WORD_1 src1_sel:DWORD
	v_and_b32_sdwa v104, v102, v98 dst_sel:DWORD dst_unused:UNUSED_PAD src0_sel:WORD_1 src1_sel:DWORD
	v_add3_u32 v100, v100, v105, s3
	v_add3_u32 v105, v103, v106, s3
	v_add3_u32 v101, v101, v107, s3
	v_cvt_pk_fp8_f32 v99, v102, v103 op_sel:[0,0,1]
	v_add3_u32 v104, v102, v104, s3
	v_and_b32_e32 v105, 0xffff0000, v105
	v_and_b32_e32 v106, 0xffff0000, v101
	v_or_b32_sdwa v101, v105, v104 dst_sel:DWORD dst_unused:UNUSED_PAD src0_sel:DWORD src1_sel:WORD_1
	v_or_b32_sdwa v100, v106, v100 dst_sel:DWORD dst_unused:UNUSED_PAD src0_sel:DWORD src1_sel:WORD_1
	global_store_dwordx2 v[90:91], v[100:101], off offset:512
	global_store_dword v[88:89], v99, off offset:256
	v_mov_b64_e32 v[100:101], v[208:209]
	v_mov_b64_e32 v[102:103], v[210:211]
	v_pk_mul_f32 v[104:105], v[86:87], v[10:11] op_sel_hi:[0,1]
	v_mov_b32_e32 v99, 0
	v_pk_mul_f32 v[106:107], v[86:87], v[12:13] op_sel_hi:[0,1]
	v_pk_mul_f32 v[100:101], v[104:105], v[100:101]
	s_nop 0
	v_cvt_pk_fp8_f32 v99, v100, v101
	v_pk_mul_f32 v[102:103], v[106:107], v[102:103]
	v_and_b32_sdwa v105, v100, v98 dst_sel:DWORD dst_unused:UNUSED_PAD src0_sel:WORD_1 src1_sel:DWORD
	v_and_b32_sdwa v106, v103, v98 dst_sel:DWORD dst_unused:UNUSED_PAD src0_sel:WORD_1 src1_sel:DWORD
	v_and_b32_sdwa v107, v101, v98 dst_sel:DWORD dst_unused:UNUSED_PAD src0_sel:WORD_1 src1_sel:DWORD
	v_and_b32_sdwa v104, v102, v98 dst_sel:DWORD dst_unused:UNUSED_PAD src0_sel:WORD_1 src1_sel:DWORD
	v_add3_u32 v100, v100, v105, s3
	v_add3_u32 v105, v103, v106, s3
	v_add3_u32 v101, v101, v107, s3
	v_cvt_pk_fp8_f32 v99, v102, v103 op_sel:[0,0,1]
	v_add3_u32 v104, v102, v104, s3
	v_and_b32_e32 v105, 0xffff0000, v105
	v_and_b32_e32 v106, 0xffff0000, v101
	v_or_b32_sdwa v101, v105, v104 dst_sel:DWORD dst_unused:UNUSED_PAD src0_sel:DWORD src1_sel:WORD_1
	v_or_b32_sdwa v100, v106, v100 dst_sel:DWORD dst_unused:UNUSED_PAD src0_sel:DWORD src1_sel:WORD_1
	global_store_dwordx2 v[90:91], v[100:101], off offset:1024
	global_store_dword v[88:89], v99, off offset:512
	v_mov_b64_e32 v[100:101], v[212:213]
	v_mov_b64_e32 v[102:103], v[214:215]
	v_pk_mul_f32 v[104:105], v[86:87], v[14:15] op_sel_hi:[0,1]
	v_mov_b32_e32 v99, 0
	v_pk_mul_f32 v[106:107], v[86:87], v[16:17] op_sel_hi:[0,1]
	v_pk_mul_f32 v[100:101], v[104:105], v[100:101]
	s_nop 0
	v_cvt_pk_fp8_f32 v99, v100, v101
	v_pk_mul_f32 v[102:103], v[106:107], v[102:103]
	v_and_b32_sdwa v105, v100, v98 dst_sel:DWORD dst_unused:UNUSED_PAD src0_sel:WORD_1 src1_sel:DWORD
	v_and_b32_sdwa v106, v103, v98 dst_sel:DWORD dst_unused:UNUSED_PAD src0_sel:WORD_1 src1_sel:DWORD
	v_and_b32_sdwa v107, v101, v98 dst_sel:DWORD dst_unused:UNUSED_PAD src0_sel:WORD_1 src1_sel:DWORD
	v_and_b32_sdwa v104, v102, v98 dst_sel:DWORD dst_unused:UNUSED_PAD src0_sel:WORD_1 src1_sel:DWORD
	v_add3_u32 v100, v100, v105, s3
	v_add3_u32 v105, v103, v106, s3
	v_add3_u32 v101, v101, v107, s3
	v_cvt_pk_fp8_f32 v99, v102, v103 op_sel:[0,0,1]
	v_add3_u32 v104, v102, v104, s3
	v_and_b32_e32 v105, 0xffff0000, v105
	v_and_b32_e32 v106, 0xffff0000, v101
	v_or_b32_sdwa v101, v105, v104 dst_sel:DWORD dst_unused:UNUSED_PAD src0_sel:DWORD src1_sel:WORD_1
	v_or_b32_sdwa v100, v106, v100 dst_sel:DWORD dst_unused:UNUSED_PAD src0_sel:DWORD src1_sel:WORD_1
	global_store_dwordx2 v[90:91], v[100:101], off offset:1536
	global_store_dword v[88:89], v99, off offset:768
	v_mov_b64_e32 v[100:101], v[216:217]
	v_mov_b64_e32 v[102:103], v[218:219]
	v_pk_mul_f32 v[104:105], v[86:87], v[18:19] op_sel_hi:[0,1]
	v_mov_b32_e32 v99, 0
	v_pk_mul_f32 v[106:107], v[86:87], v[20:21] op_sel_hi:[0,1]
	v_pk_mul_f32 v[100:101], v[104:105], v[100:101]
	s_nop 0
	v_cvt_pk_fp8_f32 v99, v100, v101
	v_pk_mul_f32 v[102:103], v[106:107], v[102:103]
	v_and_b32_sdwa v105, v100, v98 dst_sel:DWORD dst_unused:UNUSED_PAD src0_sel:WORD_1 src1_sel:DWORD
	v_and_b32_sdwa v106, v103, v98 dst_sel:DWORD dst_unused:UNUSED_PAD src0_sel:WORD_1 src1_sel:DWORD
	v_and_b32_sdwa v107, v101, v98 dst_sel:DWORD dst_unused:UNUSED_PAD src0_sel:WORD_1 src1_sel:DWORD
	v_and_b32_sdwa v104, v102, v98 dst_sel:DWORD dst_unused:UNUSED_PAD src0_sel:WORD_1 src1_sel:DWORD
	v_add3_u32 v100, v100, v105, s3
	v_add3_u32 v105, v103, v106, s3
	v_add3_u32 v101, v101, v107, s3
	v_cvt_pk_fp8_f32 v99, v102, v103 op_sel:[0,0,1]
	v_add3_u32 v104, v102, v104, s3
	v_and_b32_e32 v105, 0xffff0000, v105
	v_and_b32_e32 v106, 0xffff0000, v101
	v_or_b32_sdwa v101, v105, v104 dst_sel:DWORD dst_unused:UNUSED_PAD src0_sel:DWORD src1_sel:WORD_1
	v_or_b32_sdwa v100, v106, v100 dst_sel:DWORD dst_unused:UNUSED_PAD src0_sel:DWORD src1_sel:WORD_1
	global_store_dwordx2 v[90:91], v[100:101], off offset:2048
	global_store_dword v[88:89], v99, off offset:1024
	v_mov_b64_e32 v[100:101], v[220:221]
	v_mov_b64_e32 v[102:103], v[222:223]
	v_pk_mul_f32 v[104:105], v[86:87], v[22:23] op_sel_hi:[0,1]
	v_mov_b32_e32 v99, 0
	v_pk_mul_f32 v[106:107], v[86:87], v[24:25] op_sel_hi:[0,1]
	v_pk_mul_f32 v[100:101], v[104:105], v[100:101]
	s_nop 0
	v_cvt_pk_fp8_f32 v99, v100, v101
	v_pk_mul_f32 v[102:103], v[106:107], v[102:103]
	v_and_b32_sdwa v105, v100, v98 dst_sel:DWORD dst_unused:UNUSED_PAD src0_sel:WORD_1 src1_sel:DWORD
	v_and_b32_sdwa v106, v103, v98 dst_sel:DWORD dst_unused:UNUSED_PAD src0_sel:WORD_1 src1_sel:DWORD
	v_and_b32_sdwa v107, v101, v98 dst_sel:DWORD dst_unused:UNUSED_PAD src0_sel:WORD_1 src1_sel:DWORD
	v_and_b32_sdwa v104, v102, v98 dst_sel:DWORD dst_unused:UNUSED_PAD src0_sel:WORD_1 src1_sel:DWORD
	v_add3_u32 v100, v100, v105, s3
	v_add3_u32 v105, v103, v106, s3
	v_add3_u32 v101, v101, v107, s3
	v_cvt_pk_fp8_f32 v99, v102, v103 op_sel:[0,0,1]
	v_add3_u32 v104, v102, v104, s3
	v_and_b32_e32 v105, 0xffff0000, v105
	v_and_b32_e32 v106, 0xffff0000, v101
	v_or_b32_sdwa v101, v105, v104 dst_sel:DWORD dst_unused:UNUSED_PAD src0_sel:DWORD src1_sel:WORD_1
	v_or_b32_sdwa v100, v106, v100 dst_sel:DWORD dst_unused:UNUSED_PAD src0_sel:DWORD src1_sel:WORD_1
	global_store_dwordx2 v[90:91], v[100:101], off offset:2560
	global_store_dword v[88:89], v99, off offset:1280
	v_mov_b64_e32 v[100:101], v[224:225]
	v_mov_b64_e32 v[102:103], v[226:227]
	v_pk_mul_f32 v[104:105], v[86:87], v[26:27] op_sel_hi:[0,1]
	v_mov_b32_e32 v99, 0
	v_pk_mul_f32 v[106:107], v[86:87], v[28:29] op_sel_hi:[0,1]
	v_pk_mul_f32 v[100:101], v[104:105], v[100:101]
	s_nop 0
	v_cvt_pk_fp8_f32 v99, v100, v101
	v_pk_mul_f32 v[102:103], v[106:107], v[102:103]
	v_and_b32_sdwa v105, v100, v98 dst_sel:DWORD dst_unused:UNUSED_PAD src0_sel:WORD_1 src1_sel:DWORD
	v_and_b32_sdwa v106, v103, v98 dst_sel:DWORD dst_unused:UNUSED_PAD src0_sel:WORD_1 src1_sel:DWORD
	v_and_b32_sdwa v107, v101, v98 dst_sel:DWORD dst_unused:UNUSED_PAD src0_sel:WORD_1 src1_sel:DWORD
	v_and_b32_sdwa v104, v102, v98 dst_sel:DWORD dst_unused:UNUSED_PAD src0_sel:WORD_1 src1_sel:DWORD
	v_add3_u32 v100, v100, v105, s3
	v_add3_u32 v105, v103, v106, s3
	v_add3_u32 v101, v101, v107, s3
	v_cvt_pk_fp8_f32 v99, v102, v103 op_sel:[0,0,1]
	v_add3_u32 v104, v102, v104, s3
	v_and_b32_e32 v105, 0xffff0000, v105
	v_and_b32_e32 v106, 0xffff0000, v101
	v_or_b32_sdwa v101, v105, v104 dst_sel:DWORD dst_unused:UNUSED_PAD src0_sel:DWORD src1_sel:WORD_1
	v_or_b32_sdwa v100, v106, v100 dst_sel:DWORD dst_unused:UNUSED_PAD src0_sel:DWORD src1_sel:WORD_1
	global_store_dwordx2 v[90:91], v[100:101], off offset:3072
	global_store_dword v[88:89], v99, off offset:1536
	v_mov_b64_e32 v[100:101], v[228:229]
	v_mov_b64_e32 v[102:103], v[230:231]
	v_pk_mul_f32 v[104:105], v[86:87], v[30:31] op_sel_hi:[0,1]
	v_mov_b32_e32 v99, 0
	v_pk_mul_f32 v[106:107], v[86:87], v[32:33] op_sel_hi:[0,1]
	v_pk_mul_f32 v[100:101], v[104:105], v[100:101]
	s_nop 0
	v_cvt_pk_fp8_f32 v99, v100, v101
	v_pk_mul_f32 v[102:103], v[106:107], v[102:103]
	v_and_b32_sdwa v104, v100, v98 dst_sel:DWORD dst_unused:UNUSED_PAD src0_sel:WORD_1 src1_sel:DWORD
	v_and_b32_sdwa v105, v103, v98 dst_sel:DWORD dst_unused:UNUSED_PAD src0_sel:WORD_1 src1_sel:DWORD
	v_and_b32_sdwa v106, v101, v98 dst_sel:DWORD dst_unused:UNUSED_PAD src0_sel:WORD_1 src1_sel:DWORD
	v_cvt_pk_fp8_f32 v99, v102, v103 op_sel:[0,0,1]
	v_and_b32_sdwa v86, v102, v98 dst_sel:DWORD dst_unused:UNUSED_PAD src0_sel:WORD_1 src1_sel:DWORD
	v_add3_u32 v100, v100, v104, s3
	v_add3_u32 v104, v103, v105, s3
	v_add3_u32 v101, v101, v106, s3
	v_add3_u32 v86, v102, v86, s3
	v_and_b32_e32 v104, 0xffff0000, v104
	v_and_b32_e32 v105, 0xffff0000, v101
	v_or_b32_sdwa v101, v104, v86 dst_sel:DWORD dst_unused:UNUSED_PAD src0_sel:DWORD src1_sel:WORD_1
	v_or_b32_sdwa v100, v105, v100 dst_sel:DWORD dst_unused:UNUSED_PAD src0_sel:DWORD src1_sel:WORD_1
	global_store_dwordx2 v[90:91], v[100:101], off offset:3584
	global_store_dword v[88:89], v99, off offset:1792
	s_waitcnt vmcnt(16)
	s_cbranch_vccnz .LBB0_64
	s_cmpk_gt_i32 s0, 0x3fff
	s_cbranch_scc1 .LBB0_63
	v_lshl_add_u64 v[18:19], s[14:15], 0, v[66:67]
	v_add_co_u32_e32 v30, vcc, 0x1000, v18
	global_load_dwordx4 v[2:5], v[18:19], off
	global_load_dwordx4 v[6:9], v[18:19], off offset:1024
	global_load_dwordx4 v[10:13], v[18:19], off offset:2048
	global_load_dwordx4 v[14:17], v[18:19], off offset:3072
	v_addc_co_u32_e32 v31, vcc, 0, v19, vcc
	global_load_dwordx4 v[18:21], v[30:31], off
	global_load_dwordx4 v[22:25], v[30:31], off offset:1024
	global_load_dwordx4 v[26:29], v[30:31], off offset:2048
	s_nop 0
	global_load_dwordx4 v[30:33], v[30:31], off offset:3072
	s_branch .LBB0_63
